# final phase: hoist loop-invariant gain loads out of store loop (no vmcnt(0) per store)
# speedup vs baseline: 1.0181x; 1.0181x over previous
.LBB0_4626:
	s_or_b64 exec, exec, s[0:1]
	s_ashr_i32 s0, s3, 6
	s_add_i32 s4, s0, s78
	s_cmpk_gt_i32 s4, 0x3fff
	s_waitcnt lgkmcnt(0)
	s_barrier
	s_cbranch_scc1 .LBB0_4629
	v_and_b32_e32 v2, 63, v0
	v_lshlrev_b32_e32 v4, 4, v2
	v_lshlrev_b32_e32 v0, 2, v2
	v_mov_b32_e32 v5, 0
	v_xor_b32_e32 v56, 64, v0
	v_xor_b32_e32 v57, 0x80, v0
	v_or_b32_e32 v0, 0x1000, v4
	v_mov_b32_e32 v1, v5
	v_lshl_add_u64 v[8:9], s[70:71], 0, v[0:1]
	v_or_b32_e32 v0, 0x1400, v4
	s_add_u32 s10, s74, 0x3b400000
	v_lshl_add_u64 v[10:11], s[70:71], 0, v[0:1]
	v_or_b32_e32 v0, 0x1800, v4
	s_addc_u32 s11, s75, 0
	v_lshl_add_u64 v[12:13], s[70:71], 0, v[0:1]
	v_or_b32_e32 v0, 0x1c00, v4
	s_add_u32 s12, s74, 0x3b500000
	v_lshl_add_u64 v[14:15], s[70:71], 0, v[0:1]
	v_lshlrev_b32_e32 v0, 3, v2
	s_addc_u32 s13, s75, 0
	v_lshl_add_u64 v[2:3], s[74:75], 0, v[0:1]
	s_mov_b64 s[2:3], 0x26c00000
	s_lshl_b32 s1, s96, 4
	s_lshl_b32 s0, s0, 1
	s_ashr_i32 s5, s4, 31
	v_lshl_add_u64 v[16:17], v[2:3], 0, s[2:3]
	s_add_i32 s2, s1, s0
	s_lshl_b32 s14, s76, 4
	s_lshl_b64 s[0:1], s[4:5], 12
	s_add_u32 s0, s74, s0
	s_addc_u32 s1, s75, s1
	v_lshl_add_u64 v[0:1], s[0:1], 0, v[0:1]
	s_mov_b64 s[0:1], 0xe400000
	s_ashr_i32 s95, s94, 31
	v_lshl_add_u64 v[18:19], v[0:1], 0, s[0:1]
	s_lshl_b64 s[6:7], s[94:95], 12
	s_lshl_b64 s[0:1], s[4:5], 13
	s_add_u32 s0, s72, s0
	s_addc_u32 s1, s73, s1
	v_lshl_add_u64 v[0:1], s[0:1], 0, v[4:5]
	s_mov_b64 s[0:1], 0x1000
	v_lshl_add_u64 v[6:7], s[70:71], 0, v[4:5]
	v_lshl_add_u64 v[20:21], v[0:1], 0, s[0:1]
	s_lshl_b64 s[8:9], s[94:95], 13
	s_add_i32 s5, 0, 0x20080
	v_mov_b32_e32 v4, 0x358637bd
	s_mov_b32 s15, 0xf800000
	v_mov_b32_e32 v58, 0x260
	global_load_dwordx4 v[130:133], v[6:7], off
	global_load_dwordx4 v[134:137], v[6:7], off offset:1024
	global_load_dwordx4 v[138:141], v[6:7], off offset:2048
	global_load_dwordx4 v[142:145], v[6:7], off offset:3072
	global_load_dwordx4 v[146:149], v[8:9], off
	global_load_dwordx4 v[150:153], v[10:11], off
	global_load_dwordx4 v[154:157], v[12:13], off
	global_load_dwordx4 v[158:161], v[14:15], off
	s_waitcnt vmcnt(0)
.LBB0_4628:
	s_ashr_i32 s3, s2, 31
	s_lshl_b64 s[0:1], s[2:3], 2
	s_add_u32 s16, s10, s0
	s_addc_u32 s17, s11, s1
	global_load_dwordx2 v[22:23], v[18:19], off offset:2560
	global_load_dwordx2 v[24:25], v[18:19], off offset:3072
	global_load_dwordx2 v[30:31], v[18:19], off offset:3584
	global_load_dwordx2 v[42:43], v[18:19], off offset:1024
	global_load_dwordx2 v[46:47], v[18:19], off offset:1536
	global_load_dwordx2 v[26:27], v[18:19], off offset:2048
	global_load_dwordx2 v[52:53], v[18:19], off
	global_load_dwordx2 v[34:35], v[18:19], off offset:512
	global_load_dwordx2 v[60:61], v5, s[16:17]
	s_add_i32 s18, s2, 1
	s_ashr_i32 s19, s18, 31
	s_add_u32 s0, s12, s0
	s_addc_u32 s1, s13, s1
	global_load_dword v28, v5, s[0:1]
	s_lshl_b64 s[16:17], s[18:19], 2
	s_add_u32 s0, s12, s16
	s_addc_u32 s1, s13, s17
	global_load_dword v29, v5, s[0:1]
	s_add_i32 s4, s4, s94
	s_add_i32 s2, s2, s14
	v_lshl_add_u64 v[18:19], v[18:19], 0, s[6:7]
	s_cmpk_lt_i32 s4, 0x4000
	s_waitcnt vmcnt(0)
	v_and_b32_e32 v59, 0xffff0000, v22
	v_lshlrev_b32_e32 v36, 16, v24
	v_and_b32_e32 v114, 0xffff0000, v24
	v_lshlrev_b32_e32 v38, 16, v25
	v_and_b32_e32 v126, 0xffff0000, v25
	v_lshlrev_b32_e32 v48, 16, v27
	v_and_b32_e32 v49, 0xffff0000, v27
	v_lshlrev_b32_e32 v62, 16, v26
	v_and_b32_e32 v63, 0xffff0000, v26
	v_lshlrev_b32_e32 v26, 16, v23
	v_and_b32_e32 v27, 0xffff0000, v23
	v_lshrrev_b32_e32 v23, 18, v60
	v_lshrrev_b32_e32 v24, 18, v61
	v_and_b32_e32 v23, 0x3ffc, v23
	v_and_b32_e32 v24, 0x3ffc, v24
	v_add_u32_e32 v23, s5, v23
	v_add_u32_e32 v24, s5, v24
	ds_read_b32 v23, v23
	ds_read_b32 v37, v24
	v_lshlrev_b32_e32 v127, 16, v30
	v_and_b32_e32 v25, 0xffff0000, v30
	v_and_b32_e32 v30, 0xfffff, v60
	v_and_b32_e32 v32, 0xfffff, v61
	s_waitcnt lgkmcnt(1)
	v_add_u32_e32 v64, v23, v30
	s_waitcnt lgkmcnt(0)
	v_add_u32_e32 v66, v37, v32
	v_ashrrev_i32_e32 v65, 31, v64
	v_ashrrev_i32_e32 v67, 31, v66
	v_lshlrev_b64 v[64:65], 12, v[64:65]
	v_lshlrev_b64 v[66:67], 12, v[66:67]
	v_lshl_add_u64 v[64:65], v[16:17], 0, v[64:65]
	v_lshl_add_u64 v[66:67], v[16:17], 0, v[66:67]
	global_load_dwordx2 v[68:69], v[66:67], off offset:512
	global_load_dwordx2 v[70:71], v[64:65], off offset:512
	global_load_dwordx2 v[72:73], v[66:67], off offset:2048
	global_load_dwordx2 v[74:75], v[64:65], off offset:2048
	global_load_dwordx2 v[76:77], v[66:67], off offset:2560
	global_load_dwordx2 v[78:79], v[64:65], off offset:2560
	global_load_dwordx2 v[80:81], v[66:67], off offset:3072
	global_load_dwordx2 v[82:83], v[64:65], off offset:3072
	global_load_dwordx2 v[84:85], v[64:65], off offset:3584
	global_load_dwordx2 v[86:87], v[66:67], off offset:3584
	global_load_dwordx2 v[88:89], v[64:65], off offset:1024
	global_load_dwordx2 v[90:91], v[66:67], off offset:1024
	global_load_dwordx2 v[92:93], v[64:65], off offset:1536
	global_load_dwordx2 v[94:95], v[66:67], off offset:1536
	global_load_dwordx2 v[96:97], v[64:65], off
	s_nop 0
	global_load_dwordx2 v[64:65], v[66:67], off
	v_mov_b32_e32 v24, v29
	v_lshlrev_b32_e32 v33, 16, v31
	v_and_b32_e32 v31, 0xffff0000, v31
	v_lshlrev_b32_e32 v50, 16, v52
	v_and_b32_e32 v51, 0xffff0000, v52
	v_lshlrev_b32_e32 v52, 16, v53
	v_and_b32_e32 v53, 0xffff0000, v53
	v_lshlrev_b32_e32 v54, 16, v34
	v_and_b32_e32 v55, 0xffff0000, v34
	v_lshlrev_b32_e32 v34, 16, v35
	v_and_b32_e32 v35, 0xffff0000, v35
	v_lshlrev_b32_e32 v22, 16, v22
	v_lshlrev_b32_e32 v41, 16, v43
	v_lshlrev_b32_e32 v40, 16, v42
	v_and_b32_e32 v43, 0xffff0000, v43
	v_and_b32_e32 v42, 0xffff0000, v42
	v_lshlrev_b32_e32 v45, 16, v47
	v_lshlrev_b32_e32 v44, 16, v46
	v_and_b32_e32 v47, 0xffff0000, v47
	v_and_b32_e32 v46, 0xffff0000, v46
	v_mov_b32_e32 v61, v28
	s_waitcnt vmcnt(15)
	v_lshlrev_b32_e32 v67, 16, v68
	s_waitcnt vmcnt(14)
	v_lshlrev_b32_e32 v66, 16, v70
	v_and_b32_e32 v99, 0xffff0000, v68
	v_and_b32_e32 v98, 0xffff0000, v70
	v_lshlrev_b32_e32 v101, 16, v69
	v_lshlrev_b32_e32 v100, 16, v71
	v_and_b32_e32 v69, 0xffff0000, v69
	v_and_b32_e32 v68, 0xffff0000, v71
	s_waitcnt vmcnt(13)
	v_lshlrev_b32_e32 v71, 16, v72
	s_waitcnt vmcnt(12)
	v_lshlrev_b32_e32 v70, 16, v74
	v_and_b32_e32 v103, 0xffff0000, v72
	v_and_b32_e32 v102, 0xffff0000, v74
	s_waitcnt vmcnt(10)
	v_lshlrev_b32_e32 v104, 16, v78
	v_and_b32_e32 v106, 0xffff0000, v78
	s_waitcnt vmcnt(8)
	v_lshlrev_b32_e32 v78, 16, v82
	v_and_b32_e32 v110, 0xffff0000, v82
	s_waitcnt vmcnt(6)
	v_lshlrev_b32_e32 v115, 16, v86
	v_and_b32_e32 v32, 0xffff0000, v86
	v_lshlrev_b32_e32 v39, 16, v87
	v_and_b32_e32 v82, 0xffff0000, v87
	s_waitcnt vmcnt(4)
	v_lshlrev_b32_e32 v87, 16, v91
	v_lshlrev_b32_e32 v86, 16, v90
	v_and_b32_e32 v91, 0xffff0000, v91
	v_and_b32_e32 v90, 0xffff0000, v90
	s_waitcnt vmcnt(2)
	v_lshlrev_b32_e32 v119, 16, v95
	v_lshlrev_b32_e32 v118, 16, v94
	v_and_b32_e32 v95, 0xffff0000, v95
	v_and_b32_e32 v94, 0xffff0000, v94
	v_and_b32_e32 v121, 0xffff0000, v75
	v_lshlrev_b32_e32 v120, 16, v75
	v_and_b32_e32 v75, 0xffff0000, v73
	v_lshlrev_b32_e32 v74, 16, v73
	s_waitcnt vmcnt(1)
	v_and_b32_e32 v73, 0xffff0000, v96
	v_lshlrev_b32_e32 v72, 16, v96
	v_and_b32_e32 v125, 0xffff0000, v97
	v_lshlrev_b32_e32 v124, 16, v97
	s_waitcnt vmcnt(0)
	v_and_b32_e32 v97, 0xffff0000, v65
	v_lshlrev_b32_e32 v96, 16, v65
	v_lshlrev_b32_e32 v105, 16, v76
	v_and_b32_e32 v107, 0xffff0000, v76
	v_lshlrev_b32_e32 v108, 16, v79
	v_and_b32_e32 v76, 0xffff0000, v79
	v_lshlrev_b32_e32 v79, 16, v80
	v_and_b32_e32 v111, 0xffff0000, v80
	v_lshlrev_b32_e32 v113, 16, v81
	v_lshlrev_b32_e32 v112, 16, v83
	v_and_b32_e32 v81, 0xffff0000, v81
	v_and_b32_e32 v80, 0xffff0000, v83
	v_lshlrev_b32_e32 v83, 16, v84
	v_and_b32_e32 v23, 0xffff0000, v84
	v_lshlrev_b32_e32 v37, 16, v85
	v_and_b32_e32 v60, 0xffff0000, v85
	v_lshlrev_b32_e32 v85, 16, v89
	v_lshlrev_b32_e32 v84, 16, v88
	v_and_b32_e32 v89, 0xffff0000, v89
	v_and_b32_e32 v88, 0xffff0000, v88
	v_lshlrev_b32_e32 v117, 16, v93
	v_lshlrev_b32_e32 v116, 16, v92
	v_and_b32_e32 v93, 0xffff0000, v93
	v_and_b32_e32 v92, 0xffff0000, v92
	v_and_b32_e32 v123, 0xffff0000, v64
	v_lshlrev_b32_e32 v122, 16, v64
	v_pk_mul_f32 v[64:65], v[28:29], v[66:67]
	v_pk_mul_f32 v[66:67], v[28:29], v[98:99]
	v_pk_mul_f32 v[98:99], v[28:29], v[100:101]
	v_pk_mul_f32 v[68:69], v[28:29], v[68:69]
	v_pk_mul_f32 v[86:87], v[24:25], v[86:87] op_sel_hi:[0,1]
	v_pk_mul_f32 v[90:91], v[24:25], v[90:91] op_sel_hi:[0,1]
	v_pk_mul_f32 v[94:95], v[24:25], v[94:95] op_sel_hi:[0,1]
	v_pk_mul_f32 v[96:97], v[24:25], v[96:97] op_sel_hi:[0,1]
	v_lshlrev_b32_e32 v109, 16, v77
	v_pk_mul_f32 v[100:101], v[28:29], v[102:103]
	v_pk_mul_f32 v[102:103], v[28:29], v[106:107]
	v_pk_mul_f32 v[80:81], v[28:29], v[80:81]
	v_mul_f32_e32 v30, v29, v105
	v_pk_mul_f32 v[118:119], v[24:25], v[118:119] op_sel_hi:[0,1]
	v_pk_mul_f32 v[74:75], v[24:25], v[74:75] op_sel_hi:[0,1]
	v_pk_mul_f32 v[122:123], v[24:25], v[122:123] op_sel_hi:[0,1]
	v_mul_f32_e32 v24, v29, v79
	v_pk_fma_f32 v[84:85], v[28:29], v[84:85], v[86:87] op_sel_hi:[0,1,1]
	v_pk_fma_f32 v[86:87], v[28:29], v[88:89], v[90:91] op_sel_hi:[0,1,1]
	v_pk_fma_f32 v[90:91], v[28:29], v[92:93], v[94:95] op_sel_hi:[0,1,1]
	v_pk_fma_f32 v[92:93], v[28:29], v[124:125], v[96:97] op_sel_hi:[0,1,1]
	v_mov_b32_e32 v96, v64
	v_mov_b32_e32 v97, v66
	v_mov_b32_e32 v66, v65
	v_mov_b32_e32 v64, v98
	v_mov_b32_e32 v65, v68
	v_mov_b32_e32 v68, v99
	v_and_b32_e32 v77, 0xffff0000, v77
	v_pk_mul_f32 v[70:71], v[28:29], v[70:71]
	v_pk_mul_f32 v[106:107], v[28:29], v[108:109]
	v_pk_mul_f32 v[108:109], v[28:29], v[110:111]
	v_mul_f32_e32 v110, v28, v37
	v_mul_f32_e32 v37, v29, v39
	v_mul_f32_e32 v39, v29, v82
	v_add_f32_e32 v82, v102, v103
	v_add_f32_e32 v103, v80, v81
	v_pk_fma_f32 v[80:81], v[28:29], v[104:105], v[30:31] op_sel_hi:[1,1,0]
	v_pk_fma_f32 v[72:73], v[28:29], v[72:73], v[122:123] op_sel_hi:[0,1,1]
	v_pk_fma_f32 v[78:79], v[28:29], v[78:79], v[24:25] op_sel_hi:[1,1,0]
	v_pk_add_f32 v[66:67], v[96:97], v[66:67]
	v_pk_add_f32 v[64:65], v[64:65], v[68:69]
	v_pk_mul_f32 v[76:77], v[28:29], v[76:77]
	v_mul_f32_e32 v111, v29, v32
	v_mul_f32_e32 v32, v29, v113
	v_add_f32_e32 v102, v108, v109
	v_mov_b32_e32 v98, v70
	v_mov_b32_e32 v99, v100
	v_mov_b32_e32 v100, v71
	v_mov_b32_e32 v81, v28
	v_pk_add_f32 v[50:51], v[72:73], v[50:51]
	v_pk_add_f32 v[52:53], v[92:93], v[52:53]
	v_mov_b32_e32 v79, v110
	v_pk_add_f32 v[54:55], v[66:67], v[54:55]
	v_pk_add_f32 v[34:35], v[64:65], v[34:35]
	v_mul_f32_e32 v60, v28, v60
	v_pk_fma_f32 v[88:89], v[28:29], v[116:117], v[118:119] op_sel_hi:[0,1,1]
	v_pk_fma_f32 v[74:75], v[28:29], v[120:121], v[74:75] op_sel_hi:[0,1,1]
	v_pk_fma_f32 v[94:95], v[28:29], v[112:113], v[32:33] op_sel_hi:[1,1,0]
	v_mov_b32_e32 v70, v106
	v_mov_b32_e32 v71, v76
	v_mov_b32_e32 v76, v107
	v_add_f32_e32 v102, v102, v114
	v_pk_add_f32 v[42:43], v[86:87], v[42:43]
	v_pk_add_f32 v[46:47], v[90:91], v[46:47]
	v_pk_add_f32 v[68:69], v[98:99], v[100:101]
	v_pk_add_f32 v[72:73], v[80:81], v[22:23]
	v_pk_mul_f32 v[22:23], v[80:81], v[22:23]
	v_pk_add_f32 v[36:37], v[78:79], v[36:37]
	v_mov_b32_e32 v78, v51
	v_mov_b32_e32 v80, v53
	v_mov_b32_e32 v79, v55
	v_mov_b32_e32 v81, v35
	v_add_f32_e32 v103, v103, v126
	v_pk_add_f32 v[40:41], v[84:85], v[40:41]
	v_pk_add_f32 v[44:45], v[88:89], v[44:45]
	v_pk_add_f32 v[48:49], v[74:75], v[48:49]
	v_mov_b32_e32 v95, v60
	v_pk_add_f32 v[70:71], v[70:71], v[76:77]
	v_pk_mul_f32 v[74:75], v[42:43], v[42:43]
	v_pk_mul_f32 v[76:77], v[46:47], v[46:47]
	v_mul_f32_e32 v28, v102, v102
	v_mov_b32_e32 v66, v50
	v_mov_b32_e32 v64, v52
	v_pk_add_f32 v[62:63], v[68:69], v[62:63]
	v_mov_b32_e32 v22, v72
	v_mov_b32_e32 v110, v72
	v_mov_b32_e32 v67, v54
	v_mov_b32_e32 v65, v34
	v_pk_mul_f32 v[78:79], v[78:79], v[78:79]
	v_pk_mul_f32 v[80:81], v[80:81], v[80:81]
	v_add_f32_e32 v59, v82, v59
	v_mul_f32_e32 v60, v103, v103
	v_pk_add_f32 v[38:39], v[94:95], v[38:39]
	v_pk_add_f32 v[26:27], v[70:71], v[26:27]
	v_pk_fma_f32 v[68:69], v[40:41], v[40:41], v[74:75]
	v_pk_fma_f32 v[70:71], v[44:45], v[44:45], v[76:77]
	v_pk_mul_f32 v[76:77], v[72:73], v[72:73]
	v_pk_fma_f32 v[84:85], v[36:37], v[36:37], v[28:29]
	v_mov_b32_e32 v28, v63
	v_mov_b32_e32 v114, v63
	v_pk_add_f32 v[22:23], v[22:23], v[110:111]
	v_pk_fma_f32 v[66:67], v[66:67], v[66:67], v[78:79]
	v_pk_fma_f32 v[64:65], v[64:65], v[64:65], v[80:81]
	v_mul_f32_e32 v24, v59, v59
	v_pk_fma_f32 v[86:87], v[38:39], v[38:39], v[60:61]
	v_mov_b32_e32 v60, v62
	v_mov_b32_e32 v82, v62
	v_pk_mul_f32 v[88:89], v[26:27], v[26:27]
	v_pk_add_f32 v[68:69], v[68:69], v[68:69] op_sel:[0,1] op_sel_hi:[1,0]
	v_pk_mul_f32 v[28:29], v[28:29], v[114:115]
	v_mov_b32_e32 v77, v23
	v_pk_add_f32 v[64:65], v[66:67], v[64:65]
	v_mul_f32_e32 v30, v49, v49
	v_pk_mul_f32 v[90:91], v[60:61], v[82:83]
	v_pk_fma_f32 v[60:61], v[60:61], v[82:83], v[28:29]
	v_mov_b32_e32 v69, v29
	v_mov_b32_e32 v22, v88
	v_pk_add_f32 v[28:29], v[76:77], v[24:25]
	v_mov_b32_e32 v24, v89
	v_pk_add_f32 v[64:65], v[64:65], v[64:65] op_sel:[0,1] op_sel_hi:[1,0]
	v_pk_fma_f32 v[74:75], v[48:49], v[48:49], v[30:31] op_sel_hi:[1,1,0]
	v_pk_add_f32 v[70:71], v[70:71], v[70:71] op_sel:[0,1] op_sel_hi:[1,0]
	v_pk_add_f32 v[22:23], v[22:23], v[24:25]
	v_mov_b32_e32 v65, v91
	v_mov_b32_e32 v32, v36
	v_mov_b32_e32 v30, v38
	v_mov_b32_e32 v75, v127
	v_mov_b32_e32 v71, v127
	v_pk_add_f32 v[24:25], v[28:29], v[22:23]
	v_pk_mul_f32 v[22:23], v[28:29], v[22:23]
	v_pk_add_f32 v[64:65], v[64:65], v[68:69]
	v_pk_add_f32 v[32:33], v[36:37], v[32:33]
	v_pk_add_f32 v[30:31], v[38:39], v[30:31]
	v_pk_add_f32 v[60:61], v[60:61], v[74:75]
	v_mov_b32_e32 v25, v23
	v_pk_add_f32 v[22:23], v[64:65], v[70:71]
	v_pk_mul_f32 v[92:93], v[32:33], v[32:33]
	v_pk_mul_f32 v[94:95], v[30:31], v[30:31]
	v_pk_add_f32 v[64:65], v[22:23], v[60:61]
	v_pk_mul_f32 v[60:61], v[22:23], v[60:61]
	v_mov_b32_e32 v85, v93
	v_mov_b32_e32 v87, v95
	v_mov_b32_e32 v65, v61
	v_pk_add_f32 v[66:67], v[84:85], v[86:87]
	v_pk_add_f32 v[24:25], v[64:65], v[24:25]
	v_mov_b32_e32 v73, v59
	v_pk_add_f32 v[24:25], v[24:25], v[66:67]
	v_mov_b32_e32 v37, v102
	v_add_f32_e32 v22, v24, v25
	v_mov_b32_e32 v39, v103
	s_nop 0
	v_add_f32_dpp v22, v22, v22 quad_perm:[1,0,3,2] row_mask:0xf bank_mask:0xf bound_ctrl:1
	s_nop 1
	v_add_f32_dpp v22, v22, v22 quad_perm:[2,3,0,1] row_mask:0xf bank_mask:0xf bound_ctrl:1
	s_nop 1
	v_add_f32_dpp v22, v22, v22 row_ror:4 row_mask:0xf bank_mask:0xf bound_ctrl:1
	s_nop 1
	v_add_f32_dpp v22, v22, v22 row_ror:8 row_mask:0xf bank_mask:0xf bound_ctrl:1
	ds_bpermute_b32 v24, v56, v22
	s_waitcnt lgkmcnt(0)
	v_add_f32_e32 v22, v22, v24
	ds_bpermute_b32 v24, v57, v22
	s_waitcnt lgkmcnt(0)
	v_add_f32_e32 v22, v22, v24
	v_fmamk_f32 v22, v22, 0x3a000000, v4
	v_mul_f32_e32 v24, 0x4f800000, v22
	v_cmp_gt_f32_e32 vcc, s15, v22
	s_nop 1
	v_cndmask_b32_e32 v22, v22, v24, vcc
	v_sqrt_f32_e32 v24, v22
	s_nop 0
	v_add_u32_e32 v25, -1, v24
	v_add_u32_e32 v28, 1, v24
	v_fma_f32 v30, -v25, v24, v22
	v_fma_f32 v32, -v28, v24, v22
	v_cmp_ge_f32_e64 s[0:1], 0, v30
	s_nop 1
	v_cndmask_b32_e64 v24, v24, v25, s[0:1]
	v_cmp_lt_f32_e64 s[0:1], 0, v32
	s_nop 1
	v_cndmask_b32_e64 v24, v24, v28, s[0:1]
	v_mul_f32_e32 v25, 0x37800000, v24
	v_cndmask_b32_e32 v24, v24, v25, vcc
	v_cmp_class_f32_e32 vcc, v22, v58
	s_nop 1
	v_cndmask_b32_e32 v22, v24, v22, vcc
	v_div_scale_f32 v24, s[0:1], v22, v22, 1.0
	v_rcp_f32_e32 v28, v24
	v_div_scale_f32 v25, vcc, 1.0, v22, 1.0
	v_fma_f32 v30, -v24, v28, 1.0
	v_fmac_f32_e32 v28, v30, v28
	v_mul_f32_e32 v30, v25, v28
	v_fma_f32 v32, -v24, v30, v25
	v_fmac_f32_e32 v30, v32, v28
	v_fma_f32 v24, -v24, v30, v25
	v_div_fmas_f32 v24, v24, v28, v30
	v_div_fixup_f32 v22, v24, v22, 1.0
	v_pk_mul_f32 v[24:25], v[22:23], v[50:51] op_sel_hi:[0,1]
	v_pk_mul_f32 v[50:51], v[22:23], v[52:53] op_sel_hi:[0,1]
	v_pk_mul_f32 v[2:3], v[50:51], v[132:133]
	v_pk_mul_f32 v[0:1], v[24:25], v[130:131]
	global_store_dwordx4 v[20:21], v[0:3], off offset:-4096
	s_nop 1
	v_pk_mul_f32 v[24:25], v[22:23], v[34:35] op_sel_hi:[0,1]
	v_pk_mul_f32 v[34:35], v[22:23], v[54:55] op_sel_hi:[0,1]
	v_mov_b32_e32 v30, v33
	v_mov_b32_e32 v28, v23
	v_pk_mul_f32 v[0:1], v[34:35], v[134:135]
	v_pk_mul_f32 v[2:3], v[24:25], v[136:137]
	global_store_dwordx4 v[20:21], v[0:3], off offset:-3072
	s_nop 1
	v_mov_b32_e32 v24, v40
	v_mov_b32_e32 v25, v42
	v_mov_b32_e32 v42, v41
	v_pk_mul_f32 v[24:25], v[22:23], v[24:25] op_sel_hi:[0,1]
	v_pk_mul_f32 v[34:35], v[22:23], v[42:43] op_sel_hi:[0,1]
	v_pk_mul_f32 v[0:1], v[24:25], v[138:139]
	v_pk_mul_f32 v[2:3], v[34:35], v[140:141]
	global_store_dwordx4 v[20:21], v[0:3], off offset:-2048
	s_nop 1
	v_mov_b32_e32 v24, v44
	v_mov_b32_e32 v25, v46
	v_mov_b32_e32 v46, v45
	v_pk_mul_f32 v[24:25], v[22:23], v[24:25] op_sel_hi:[0,1]
	v_pk_mul_f32 v[34:35], v[22:23], v[46:47] op_sel_hi:[0,1]
	v_pk_mul_f32 v[0:1], v[24:25], v[142:143]
	v_pk_mul_f32 v[2:3], v[34:35], v[144:145]
	global_store_dwordx4 v[20:21], v[0:3], off offset:-1024
	s_nop 1
	v_pk_mul_f32 v[24:25], v[22:23], v[48:49] op_sel_hi:[0,1]
	v_pk_mul_f32 v[34:35], v[22:23], v[62:63] op_sel_hi:[0,1]
	v_pk_mul_f32 v[0:1], v[34:35], v[146:147]
	v_pk_mul_f32 v[2:3], v[24:25], v[148:149]
	global_store_dwordx4 v[20:21], v[0:3], off
	s_nop 1
	v_pk_mul_f32 v[24:25], v[22:23], v[26:27] op_sel_hi:[0,1]
	v_pk_mul_f32 v[26:27], v[22:23], v[72:73] op_sel_hi:[0,1]
	v_pk_mul_f32 v[0:1], v[26:27], v[150:151]
	v_pk_mul_f32 v[2:3], v[24:25], v[152:153]
	global_store_dwordx4 v[20:21], v[0:3], off offset:1024
	s_nop 1
	v_pk_mul_f32 v[24:25], v[22:23], v[38:39] op_sel_hi:[0,1]
	v_pk_mul_f32 v[26:27], v[22:23], v[36:37] op_sel_hi:[0,1]
	v_pk_mul_f32 v[0:1], v[26:27], v[154:155]
	v_pk_mul_f32 v[2:3], v[24:25], v[156:157]
	global_store_dwordx4 v[20:21], v[0:3], off offset:2048
	s_nop 1
	v_pk_mul_f32 v[24:25], v[22:23], v[28:29] op_sel_hi:[0,1]
	v_pk_mul_f32 v[22:23], v[22:23], v[30:31] op_sel_hi:[0,1]
	v_pk_mul_f32 v[0:1], v[24:25], v[158:159]
	v_pk_mul_f32 v[2:3], v[22:23], v[160:161]
	global_store_dwordx4 v[20:21], v[0:3], off offset:3072
	s_nop 1
	v_lshl_add_u64 v[20:21], v[20:21], 0, s[8:9]
	s_cbranch_scc1 .LBB0_4628
